# v045 with the fused conversion's loads issued right after each tile's last MFMA cluster, before the alignment barrier
# baseline (speedup 1.0000x reference)
.LBB0_1249:
	s_ashr_i32 s73, s72, 31
	s_lshl_b64 s[4:5], s[72:73], 18
	s_add_u32 s24, s8, s4
	s_addc_u32 s25, s9, s5
	s_waitcnt vmcnt(8)
	s_and_b64 s[0:1], s[0:1], exec
	s_waitcnt lgkmcnt(0)
	s_cselect_b32 s0, s24, s74
	s_cselect_b32 s1, s25, s75
	s_add_u32 s4, s0, 0x80
	s_addc_u32 s5, s1, 0
	s_barrier
	s_setprio 1
	s_waitcnt lgkmcnt(0)
	v_mfma_f32_16x16x128_f8f6f4 v[66:69], v[18:25], v[58:65], v[66:69]
	v_mfma_f32_16x16x128_f8f6f4 v[70:73], v[26:33], v[58:65], v[70:73]
	v_mfma_f32_16x16x128_f8f6f4 v[74:77], v[18:25], v[50:57], v[74:77]
	v_mfma_f32_16x16x128_f8f6f4 v[78:81], v[26:33], v[50:57], v[78:81]
	v_mfma_f32_16x16x128_f8f6f4 v[82:85], v[18:25], v[42:49], v[82:85]
	v_mfma_f32_16x16x128_f8f6f4 v[146:149], v[26:33], v[42:49], v[150:153]
	v_mfma_f32_16x16x128_f8f6f4 v[150:153], v[18:25], v[34:41], v[154:157]
	v_mfma_f32_16x16x128_f8f6f4 v[154:157], v[26:33], v[34:41], v[158:161]
	s_setprio 0
	s_setprio 1
	v_mfma_f32_16x16x128_f8f6f4 v[158:161], v[2:9], v[58:65], v[162:165]
	v_mfma_f32_16x16x128_f8f6f4 v[162:165], v[10:17], v[58:65], v[166:169]
	v_mfma_f32_16x16x128_f8f6f4 v[166:169], v[2:9], v[50:57], v[170:173]
	v_mfma_f32_16x16x128_f8f6f4 v[170:173], v[10:17], v[50:57], v[174:177]
	v_mfma_f32_16x16x128_f8f6f4 v[174:177], v[2:9], v[42:49], v[178:181]
	v_mfma_f32_16x16x128_f8f6f4 v[178:181], v[10:17], v[42:49], v[182:185]
	v_mfma_f32_16x16x128_f8f6f4 v[182:185], v[2:9], v[34:41], v[186:189]
	v_mfma_f32_16x16x128_f8f6f4 v[186:189], v[10:17], v[34:41], v[190:193]
	s_setprio 0
	s_barrier
	s_mov_b64 s[74:75], s[0:1]
	v_mov_b32_e32 v130, v194
	s_mov_b32 m0, s12
	ds_read_b128 v[34:37], v199 offset:16384
	ds_read_b128 v[38:41], v199 offset:17408
	ds_read_b128 v[42:45], v199 offset:18432
	ds_read_b128 v[46:49], v199 offset:19456
	ds_read_b128 v[50:53], v199 offset:20480
	ds_read_b128 v[54:57], v199 offset:21504
	ds_read_b128 v[58:61], v199 offset:22528
	ds_read_b128 v[62:65], v199 offset:23552
	s_nop 0
	global_load_lds_dwordx4 v130, s[74:75]
	s_add_u32 s74, s0, 0x20000
	s_addc_u32 s75, s1, 0
	v_mov_b32_e32 v130, v194
	s_mov_b32 m0, s13
	s_nop 0
	global_load_lds_dwordx4 v130, s[74:75]
	s_add_u32 s74, s0, 0x8000
	s_addc_u32 s75, s1, 0
	v_mov_b32_e32 v130, v194
	s_mov_b32 m0, s14
	s_nop 0
	global_load_lds_dwordx4 v130, s[74:75]
	s_add_u32 s74, s0, 0x28000
	s_addc_u32 s75, s1, 0
	v_mov_b32_e32 v130, v194
	s_mov_b32 m0, s15
	s_nop 0
	global_load_lds_dwordx4 v130, s[74:75]
	s_mov_b64 s[74:75], s[42:43]
	v_mov_b32_e32 v130, v195
	s_mov_b32 m0, s10
	s_nop 0
	global_load_lds_dwordx4 v130, s[74:75]
	v_mov_b32_e32 v130, v196
	s_mov_b32 m0, s16
	s_nop 0
	global_load_lds_dwordx4 v130, s[74:75]
	s_waitcnt vmcnt(8)
	s_waitcnt lgkmcnt(0)
	s_barrier
	s_setprio 1
	s_waitcnt lgkmcnt(0)
	v_mfma_f32_16x16x128_f8f6f4 v[190:193], v[18:25], v[34:41], v[202:205]
	v_mfma_f32_16x16x128_f8f6f4 v[202:205], v[26:33], v[34:41], v[208:211]
	v_mfma_f32_16x16x128_f8f6f4 v[208:211], v[18:25], v[42:49], v[212:215]
	v_mfma_f32_16x16x128_f8f6f4 v[212:215], v[26:33], v[42:49], v[216:219]
	v_mfma_f32_16x16x128_f8f6f4 v[216:219], v[18:25], v[50:57], v[220:223]
	v_mfma_f32_16x16x128_f8f6f4 v[220:223], v[26:33], v[50:57], v[86:89]
	v_mfma_f32_16x16x128_f8f6f4 v[224:227], v[18:25], v[58:65], v[90:93]
	v_mfma_f32_16x16x128_f8f6f4 v[228:231], v[26:33], v[58:65], v[94:97]
	s_setprio 0
	s_setprio 1
	v_mfma_f32_16x16x128_f8f6f4 v[234:237], v[2:9], v[34:41], v[98:101]
	v_mfma_f32_16x16x128_f8f6f4 v[238:241], v[10:17], v[34:41], v[102:105]
	v_mfma_f32_16x16x128_f8f6f4 v[242:245], v[2:9], v[42:49], v[106:109]
	v_mfma_f32_16x16x128_f8f6f4 v[246:249], v[10:17], v[42:49], v[110:113]
	v_mfma_f32_16x16x128_f8f6f4 v[86:89], v[2:9], v[50:57], v[114:117]
	v_mfma_f32_16x16x128_f8f6f4 v[54:57], v[10:17], v[50:57], v[118:121]
	v_mfma_f32_16x16x128_f8f6f4 v[90:93], v[2:9], v[58:65], v[122:125]
	v_mfma_f32_16x16x128_f8f6f4 v[62:65], v[10:17], v[58:65], v[126:129]
	s_setprio 0
	s_barrier
	ds_read_b128 v[2:5], v200 offset:32768
	ds_read_b128 v[6:9], v200 offset:33792
	ds_read_b128 v[14:17], v200 offset:34816
	ds_read_b128 v[18:21], v200 offset:35840
	ds_read_b128 v[130:133], v200 offset:49152
	ds_read_b128 v[134:137], v200 offset:50176
	ds_read_b128 v[138:141], v200 offset:51200
	ds_read_b128 v[142:145], v200 offset:52224
	s_mov_b64 s[74:75], s[42:43]
	v_mov_b32_e32 v10, v197
	s_mov_b32 m0, s17
	ds_read_b128 v[22:25], v199 offset:32768
	ds_read_b128 v[26:29], v199 offset:33792
	ds_read_b128 v[30:33], v199 offset:34816
	ds_read_b128 v[34:37], v199 offset:35840
	ds_read_b128 v[38:41], v199 offset:36864
	ds_read_b128 v[42:45], v199 offset:37888
	ds_read_b128 v[46:49], v199 offset:38912
	ds_read_b128 v[50:53], v199 offset:39936
	s_nop 0
	global_load_lds_dwordx4 v10, s[74:75]
	v_mov_b32_e32 v10, v198
	s_mov_b32 m0, s26
	s_nop 0
	global_load_lds_dwordx4 v10, s[74:75]
	s_waitcnt vmcnt(8)
	s_waitcnt lgkmcnt(0)
	s_barrier
	s_setprio 1
	s_waitcnt lgkmcnt(0)
	v_mfma_f32_16x16x128_f8f6f4 v[122:125], v[2:9], v[22:29], v[66:69]
	v_mfma_f32_16x16x128_f8f6f4 v[118:121], v[14:21], v[22:29], v[70:73]
	v_mfma_f32_16x16x128_f8f6f4 v[106:109], v[2:9], v[30:37], v[74:77]
	v_mfma_f32_16x16x128_f8f6f4 v[102:105], v[14:21], v[30:37], v[78:81]
	v_mfma_f32_16x16x128_f8f6f4 v[58:61], v[2:9], v[38:45], v[82:85]
	v_mfma_f32_16x16x128_f8f6f4 v[10:13], v[14:21], v[38:45], v[146:149]
	v_mfma_f32_16x16x128_f8f6f4 v[74:77], v[2:9], v[46:53], v[150:153]
	v_mfma_f32_16x16x128_f8f6f4 v[70:73], v[14:21], v[46:53], v[154:157]
	s_setprio 0
	s_setprio 1
	v_mfma_f32_16x16x128_f8f6f4 v[126:129], v[130:137], v[22:29], v[158:161]
	v_mfma_f32_16x16x128_f8f6f4 v[114:117], v[138:145], v[22:29], v[162:165]
	v_mfma_f32_16x16x128_f8f6f4 v[110:113], v[130:137], v[30:37], v[166:169]
	v_mfma_f32_16x16x128_f8f6f4 v[98:101], v[138:145], v[30:37], v[170:173]
	v_mfma_f32_16x16x128_f8f6f4 v[94:97], v[130:137], v[38:45], v[174:177]
	v_mfma_f32_16x16x128_f8f6f4 v[82:85], v[138:145], v[38:45], v[178:181]
	v_mfma_f32_16x16x128_f8f6f4 v[78:81], v[130:137], v[46:53], v[182:185]
	v_mfma_f32_16x16x128_f8f6f4 v[66:69], v[138:145], v[46:53], v[186:189]
	s_setprio 0
	s_barrier
	v_mov_b32_e32 v22, v194
	s_mov_b32 m0, s28
	ds_read_b128 v[30:33], v199 offset:49152
	ds_read_b128 v[34:37], v199 offset:50176
	ds_read_b128 v[146:149], v199 offset:51200
	ds_read_b128 v[150:153], v199 offset:52224
	ds_read_b128 v[154:157], v199 offset:53248
	ds_read_b128 v[158:161], v199 offset:54272
	ds_read_b128 v[162:165], v199 offset:55296
	ds_read_b128 v[166:169], v199 offset:56320
	s_nop 0
	global_load_lds_dwordx4 v22, s[4:5]
	s_add_u32 s4, s0, 0x20080
	s_addc_u32 s5, s1, 0
	v_mov_b32_e32 v22, v194
	s_mov_b32 m0, s29
	s_nop 0
	global_load_lds_dwordx4 v22, s[4:5]
	s_add_u32 s4, s0, 0x8080
	s_addc_u32 s5, s1, 0
	v_mov_b32_e32 v22, v194
	s_mov_b32 m0, s34
	s_add_u32 s0, s0, 0x28080
	global_load_lds_dwordx4 v22, s[4:5]
	s_addc_u32 s1, s1, 0
	v_mov_b32_e32 v22, v194
	s_mov_b32 m0, s35
	s_nop 0
	global_load_lds_dwordx4 v22, s[0:1]
	s_mov_b64 s[0:1], s[52:53]
	v_mov_b32_e32 v22, v195
	s_mov_b32 m0, s30
	s_nop 0
	global_load_lds_dwordx4 v22, s[0:1]
	v_mov_b32_e32 v22, v196
	s_mov_b32 m0, s31
	s_nop 0
	global_load_lds_dwordx4 v22, s[0:1]
	s_waitcnt vmcnt(8)
	s_waitcnt lgkmcnt(0)
	s_barrier
	s_setprio 1
	s_waitcnt lgkmcnt(0)
	v_mfma_f32_16x16x128_f8f6f4 v[178:181], v[2:9], v[30:37], v[190:193]
	v_mfma_f32_16x16x128_f8f6f4 v[174:177], v[14:21], v[30:37], v[202:205]
	v_mfma_f32_16x16x128_f8f6f4 v[42:45], v[2:9], v[146:153], v[208:211]
	v_mfma_f32_16x16x128_f8f6f4 v[38:41], v[14:21], v[146:153], v[212:215]
	v_mfma_f32_16x16x128_f8f6f4 v[26:29], v[2:9], v[154:161], v[216:219]
	v_mfma_f32_16x16x128_f8f6f4 v[22:25], v[14:21], v[154:161], v[220:223]
	v_mfma_f32_16x16x128_f8f6f4 v[170:173], v[2:9], v[162:169], v[224:227]
	v_mfma_f32_16x16x128_f8f6f4 v[6:9], v[14:21], v[162:169], v[228:231]
	s_setprio 0
	s_setprio 1
	v_mfma_f32_16x16x128_f8f6f4 v[182:185], v[130:137], v[30:37], v[234:237]
	v_mfma_f32_16x16x128_f8f6f4 v[50:53], v[138:145], v[30:37], v[238:241]
	v_mfma_f32_16x16x128_f8f6f4 v[46:49], v[130:137], v[146:153], v[242:245]
	v_mfma_f32_16x16x128_f8f6f4 v[34:37], v[138:145], v[146:153], v[246:249]
	v_mfma_f32_16x16x128_f8f6f4 v[30:33], v[130:137], v[154:161], v[86:89]
	v_mfma_f32_16x16x128_f8f6f4 v[18:21], v[138:145], v[154:161], v[54:57]
	v_mfma_f32_16x16x128_f8f6f4 v[14:17], v[130:137], v[162:169], v[90:93]
	v_mfma_f32_16x16x128_f8f6f4 v[2:5], v[138:145], v[162:169], v[62:65]
	s_setprio 0
	s_nop 7
	s_mov_b32 s100, -1
	v_readlane_b32 s23, v255, 55
	s_lshr_b32 s73, s77, 8
	s_cmp_lt_u32 s23, 3
	s_cbranch_scc0 .Lfz_s_skip
	s_cmp_le_u32 s73, 12
	s_cbranch_scc0 .Lfz_s_skip
	s_add_i32 s73, s73, -1
	s_lshl_b32 s73, s73, 11
	s_lshl_b32 s74, s88, 3
	s_add_i32 s73, s73, s74
	v_lshrrev_b32_e32 v224, 6, v0
	v_readlane_b32 s4, v253, 0
	v_readlane_b32 s5, v253, 1
	v_readfirstlane_b32 s74, v224
	s_add_i32 s100, s73, s74
	s_lshr_b32 s73, s100, 9
	s_mul_i32 s74, s73, 0xaaab
	s_lshr_b32 s74, s74, 17
	s_mul_i32 s75, s74, 3
	s_sub_i32 s73, s73, s75
	s_add_i32 s23, s23, 1
	s_lshl_b32 s23, s23, 4
	s_add_i32 s23, s23, s74
	s_lshl_b32 s75, s73, 3
	s_add_i32 s75, s75, 0x80
	s_load_dwordx2 s[4:5], s[4:5], s75
	s_and_b32 s74, s100, 0x1ff
	s_lshr_b32 s75, s74, 5
	s_lshl_b32 s75, s75, 19
	s_and_b32 s101, s74, 31
	s_lshl_b32 s101, s101, 8
	s_or_b32 s75, s75, s101
	s_lshr_b32 s101, s74, 4
	s_lshl_b32 s101, s101, 18
	s_and_b32 s74, s74, 15
	s_lshl_b32 s74, s74, 8
	s_or_b32 s74, s74, s101
	s_cmp_lt_u32 s73, 2
	s_cselect_b32 s75, s75, s74
	s_cselect_b32 s101, 17, 16
	s_mov_b32 s73, 0x1000
	s_cselect_b32 s73, 0x2000, s73
	s_lshl_b32 s74, s23, 23
	s_add_u32 s75, s75, s74
	v_bfe_u32 v224, v0, 4, 2
	v_and_b32_e32 v225, 15, v0
	v_lshlrev_b32_e32 v224, s101, v224
	v_lshl_or_b32 v201, v225, 4, v224
	s_waitcnt lgkmcnt(0)
	s_add_u32 s4, s4, s75
	s_addc_u32 s5, s5, 0
	global_load_dwordx4 v[134:137], v201, s[4:5] nt
	s_add_u32 s4, s4, s73
	s_addc_u32 s5, s5, 0
	global_load_dwordx4 v[138:141], v201, s[4:5] nt
	s_add_u32 s4, s4, s73
	s_addc_u32 s5, s5, 0
	global_load_dwordx4 v[142:145], v201, s[4:5] nt
	s_add_u32 s4, s4, s73
	s_addc_u32 s5, s5, 0
	global_load_dwordx4 v[146:149], v201, s[4:5] nt
	s_add_u32 s4, s4, s73
	s_addc_u32 s5, s5, 0
	global_load_dwordx4 v[150:153], v201, s[4:5] nt
	s_add_u32 s4, s4, s73
	s_addc_u32 s5, s5, 0
	global_load_dwordx4 v[154:157], v201, s[4:5] nt
	s_add_u32 s4, s4, s73
	s_addc_u32 s5, s5, 0
	global_load_dwordx4 v[158:161], v201, s[4:5] nt
	s_add_u32 s4, s4, s73
	s_addc_u32 s5, s5, 0
	global_load_dwordx4 v[162:165], v201, s[4:5] nt
	s_add_u32 s4, s4, s73
	s_addc_u32 s5, s5, 0
	global_load_dwordx4 v[166:169], v201, s[4:5] nt
	s_add_u32 s4, s4, s73
	s_addc_u32 s5, s5, 0
	global_load_dwordx4 v[186:189], v201, s[4:5] nt
	s_add_u32 s4, s4, s73
	s_addc_u32 s5, s5, 0
	global_load_dwordx4 v[190:193], v201, s[4:5] nt
	s_add_u32 s4, s4, s73
	s_addc_u32 s5, s5, 0
	global_load_dwordx4 v[208:211], v201, s[4:5] nt
	s_add_u32 s4, s4, s73
	s_addc_u32 s5, s5, 0
	global_load_dwordx4 v[212:215], v201, s[4:5] nt
	s_add_u32 s4, s4, s73
	s_addc_u32 s5, s5, 0
	global_load_dwordx4 v[216:219], v201, s[4:5] nt
	s_add_u32 s4, s4, s73
	s_addc_u32 s5, s5, 0
	global_load_dwordx4 v[220:223], v201, s[4:5] nt
	s_add_u32 s4, s4, s73
	s_addc_u32 s5, s5, 0
	global_load_dwordx4 v[234:237], v201, s[4:5] nt
.Lfz_s_skip:
	s_barrier
	s_andn2_b64 vcc, exec, s[58:59]
	s_cbranch_vccnz .LBB0_1251
	s_barrier
